# speedup vs baseline: 1.0101x; 1.0101x over previous
.Lred_skip_0:
	s_nop 5
	v_med3_f32 v120, v120, s55, v232
	v_med3_f32 v121, v121, s55, v232
	v_mfma_f32_16x16x32_bf16 v[130:133], v[102:105], v[134:137], v[130:133]
	v_exp_f32_e32 v126, v126
	v_exp_f32_e32 v127, v127
	v_mfma_f32_16x16x32_bf16 v[130:133], v[106:109], v[138:141], v[130:133]
	v_exp_f32_e32 v116, v116
	v_exp_f32_e32 v117, v117
	v_exp_f32_e32 v120, v120
	v_exp_f32_e32 v121, v121
	v_med3_f32 v122, v122, s55, v232
	v_med3_f32 v123, v123, s55, v232
	v_pk_add_f32 v[126:127], v[126:127], 1.0 op_sel_hi:[1,0]
	v_pk_add_f32 v[134:135], v[120:121], 1.0 op_sel_hi:[1,0]
	v_pk_add_f32 v[116:117], v[116:117], 1.0 op_sel_hi:[1,0]
	v_pk_add_f32 v[120:121], v[120:121], 1.0 op_sel_hi:[1,0] neg_lo:[1,0] neg_hi:[1,0]
	v_exp_f32_e32 v128, v128
	v_exp_f32_e32 v129, v129
	v_exp_f32_e32 v118, v118
	v_exp_f32_e32 v119, v119
	v_exp_f32_e32 v122, v122
	v_exp_f32_e32 v123, v123
	v_pk_mul_f32 v[126:127], v[126:127], v[134:135]
	v_exp_f32_e32 v130, v130
	v_exp_f32_e32 v131, v131
	v_pk_add_f32 v[128:129], v[128:129], 1.0 op_sel_hi:[1,0]
	v_pk_add_f32 v[136:137], v[122:123], 1.0 op_sel_hi:[1,0]
	v_pk_add_f32 v[118:119], v[118:119], 1.0 op_sel_hi:[1,0]
	v_pk_add_f32 v[122:123], v[122:123], 1.0 op_sel_hi:[1,0] neg_lo:[1,0] neg_hi:[1,0]
	v_rcp_f32_e32 v126, v126
	v_rcp_f32_e32 v127, v127
	v_rcp_f32_e32 v116, v116
	v_rcp_f32_e32 v117, v117
	v_pk_mul_f32 v[128:129], v[128:129], v[136:137]
	v_exp_f32_e32 v132, v132
	v_exp_f32_e32 v133, v133
	v_pk_mul_f32 v[120:121], v[120:121], v[126:127]
	v_pk_add_f32 v[130:131], v[130:131], 1.0 op_sel_hi:[1,0]
	v_rcp_f32_e32 v128, v128
	v_rcp_f32_e32 v129, v129
	v_rcp_f32_e32 v118, v118
	v_rcp_f32_e32 v119, v119
	v_pk_fma_f32 v[168:169], v[168:169], v[116:117], v[120:121]
	v_pk_mul_f32 v[122:123], v[122:123], v[128:129]
	v_pk_add_f32 v[132:133], v[132:133], 1.0 op_sel_hi:[1,0]
	v_pk_mul_f32 v[134:135], v[168:169], s[78:79]
	v_pk_fma_f32 v[170:171], v[170:171], v[118:119], v[122:123]
	v_med3_f32 v134, v134, s55, v232
	v_med3_f32 v135, v135, s55, v232
	v_pk_mul_f32 v[136:137], v[170:171], s[78:79]
	v_lshl_add_u64 v[122:123], v[166:167], 1, s[30:31]
	v_exp_f32_e32 v134, v134
	v_exp_f32_e32 v135, v135
	v_med3_f32 v136, v136, s55, v232
	v_med3_f32 v137, v137, s55, v232
	v_pk_add_f32 v[126:127], v[134:135], 1.0 op_sel_hi:[1,0]
	v_pk_add_f32 v[134:135], v[134:135], 1.0 op_sel_hi:[1,0] neg_lo:[1,0] neg_hi:[1,0]
	v_exp_f32_e32 v136, v136
	v_exp_f32_e32 v137, v137
	v_pk_mul_f32 v[130:131], v[130:131], v[126:127]
	v_pk_add_f32 v[128:129], v[136:137], 1.0 op_sel_hi:[1,0]
	v_pk_add_f32 v[136:137], v[136:137], 1.0 op_sel_hi:[1,0] neg_lo:[1,0] neg_hi:[1,0]
	v_rcp_f32_e32 v130, v130
	v_rcp_f32_e32 v131, v131
	v_pk_mul_f32 v[132:133], v[132:133], v[128:129]
	v_pk_mul_f32 v[134:135], v[134:135], v[130:131]
	v_rcp_f32_e32 v132, v132
	v_rcp_f32_e32 v133, v133
	v_cvt_pk_bf16_f32 v120, v134, v135
	v_pk_mul_f32 v[136:137], v[136:137], v[132:133]
	v_pk_mul_f32 v[134:135], v[162:163], v[134:135]
	v_cvt_pk_bf16_f32 v121, v136, v137
	v_cvt_pk_bf16_f32 v116, v134, v135
	v_pk_mul_f32 v[136:137], v[164:165], v[136:137]
	global_store_dwordx2 v[122:123], v[120:121], off
	v_cvt_pk_bf16_f32 v117, v136, v137
	ds_write_b64 v205, v[116:117] offset:4608
	s_and_b64 s[72:73], exec, s[6:7]
	s_cbranch_scc1 .Lpf_skip_1
	ds_read_b128 v[250:253], v199 offset:9216
	ds_read_b128 v[120:123], v198 offset:57600
	ds_read_b128 v[124:127], v199 offset:9344
	ds_read_b128 v[246:249], v199 offset:9280
	ds_read_b128 v[128:131], v199 offset:9408

.Lred_skip_1:
	s_nop 5
	v_med3_f32 v120, v120, s55, v232
	v_med3_f32 v121, v121, s55, v232
	v_mfma_f32_16x16x32_bf16 v[130:133], v[102:105], v[134:137], v[130:133]
	v_exp_f32_e32 v126, v126
	v_exp_f32_e32 v127, v127
	v_mfma_f32_16x16x32_bf16 v[130:133], v[106:109], v[138:141], v[130:133]
	v_exp_f32_e32 v116, v116
	v_exp_f32_e32 v117, v117
	v_exp_f32_e32 v120, v120
	v_exp_f32_e32 v121, v121
	v_med3_f32 v122, v122, s55, v232
	v_med3_f32 v123, v123, s55, v232
	v_pk_add_f32 v[126:127], v[126:127], 1.0 op_sel_hi:[1,0]
	v_pk_add_f32 v[134:135], v[120:121], 1.0 op_sel_hi:[1,0]
	v_pk_add_f32 v[116:117], v[116:117], 1.0 op_sel_hi:[1,0]
	v_pk_add_f32 v[120:121], v[120:121], 1.0 op_sel_hi:[1,0] neg_lo:[1,0] neg_hi:[1,0]
	v_exp_f32_e32 v128, v128
	v_exp_f32_e32 v129, v129
	v_exp_f32_e32 v118, v118
	v_exp_f32_e32 v119, v119
	v_exp_f32_e32 v122, v122
	v_exp_f32_e32 v123, v123
	v_pk_mul_f32 v[126:127], v[126:127], v[134:135]
	v_exp_f32_e32 v130, v130
	v_exp_f32_e32 v131, v131
	v_pk_add_f32 v[128:129], v[128:129], 1.0 op_sel_hi:[1,0]
	v_pk_add_f32 v[136:137], v[122:123], 1.0 op_sel_hi:[1,0]
	v_pk_add_f32 v[118:119], v[118:119], 1.0 op_sel_hi:[1,0]
	v_pk_add_f32 v[122:123], v[122:123], 1.0 op_sel_hi:[1,0] neg_lo:[1,0] neg_hi:[1,0]
	v_rcp_f32_e32 v126, v126
	v_rcp_f32_e32 v127, v127
	v_rcp_f32_e32 v116, v116
	v_rcp_f32_e32 v117, v117
	v_pk_mul_f32 v[128:129], v[128:129], v[136:137]
	v_exp_f32_e32 v132, v132
	v_exp_f32_e32 v133, v133
	v_pk_mul_f32 v[120:121], v[120:121], v[126:127]
	v_pk_add_f32 v[130:131], v[130:131], 1.0 op_sel_hi:[1,0]
	v_rcp_f32_e32 v128, v128
	v_rcp_f32_e32 v129, v129
	v_rcp_f32_e32 v118, v118
	v_rcp_f32_e32 v119, v119
	v_pk_fma_f32 v[168:169], v[168:169], v[116:117], v[120:121]
	v_pk_mul_f32 v[122:123], v[122:123], v[128:129]
	v_pk_add_f32 v[132:133], v[132:133], 1.0 op_sel_hi:[1,0]
	v_pk_mul_f32 v[134:135], v[168:169], s[78:79]
	v_pk_fma_f32 v[170:171], v[170:171], v[118:119], v[122:123]
	v_med3_f32 v134, v134, s55, v232
	v_med3_f32 v135, v135, s55, v232
	v_pk_mul_f32 v[136:137], v[170:171], s[78:79]
	v_add_u32_e32 v122, 0x80, v166
	v_mov_b32_e32 v123, v114
	v_lshl_add_u64 v[122:123], v[122:123], 1, s[30:31]
	v_exp_f32_e32 v134, v134
	v_exp_f32_e32 v135, v135
	v_med3_f32 v136, v136, s55, v232
	v_med3_f32 v137, v137, s55, v232
	v_pk_add_f32 v[126:127], v[134:135], 1.0 op_sel_hi:[1,0]
	v_pk_add_f32 v[134:135], v[134:135], 1.0 op_sel_hi:[1,0] neg_lo:[1,0] neg_hi:[1,0]
	v_exp_f32_e32 v136, v136
	v_exp_f32_e32 v137, v137
	v_pk_mul_f32 v[130:131], v[130:131], v[126:127]
	v_pk_add_f32 v[128:129], v[136:137], 1.0 op_sel_hi:[1,0]
	v_pk_add_f32 v[136:137], v[136:137], 1.0 op_sel_hi:[1,0] neg_lo:[1,0] neg_hi:[1,0]
	v_rcp_f32_e32 v130, v130
	v_rcp_f32_e32 v131, v131
	v_pk_mul_f32 v[132:133], v[132:133], v[128:129]
	v_pk_mul_f32 v[134:135], v[134:135], v[130:131]
	v_rcp_f32_e32 v132, v132
	v_rcp_f32_e32 v133, v133
	v_cvt_pk_bf16_f32 v120, v134, v135
	v_pk_mul_f32 v[136:137], v[136:137], v[132:133]
	v_pk_mul_f32 v[134:135], v[162:163], v[134:135]
	v_cvt_pk_bf16_f32 v121, v136, v137
	v_cvt_pk_bf16_f32 v116, v134, v135
	v_pk_mul_f32 v[136:137], v[164:165], v[136:137]
	global_store_dwordx2 v[122:123], v[120:121], off
	v_cvt_pk_bf16_f32 v117, v136, v137
	ds_write_b64 v205, v[116:117]
	s_and_b64 s[72:73], exec, s[6:7]
	s_cbranch_scc1 .Lpf_skip_2
	ds_read_b128 v[250:253], v199 offset:9216
	ds_read_b128 v[120:123], v198 offset:57600
	ds_read_b128 v[124:127], v199 offset:9344
	ds_read_b128 v[246:249], v199 offset:9280
	ds_read_b128 v[128:131], v199 offset:9408

.Lred_skip_2:
	s_nop 5
	v_med3_f32 v120, v120, s55, v232
	v_med3_f32 v121, v121, s55, v232
	v_mfma_f32_16x16x32_bf16 v[130:133], v[102:105], v[134:137], v[130:133]
	v_exp_f32_e32 v126, v126
	v_exp_f32_e32 v127, v127
	v_mfma_f32_16x16x32_bf16 v[130:133], v[106:109], v[138:141], v[130:133]
	v_exp_f32_e32 v116, v116
	v_exp_f32_e32 v117, v117
	v_exp_f32_e32 v120, v120
	v_exp_f32_e32 v121, v121
	v_med3_f32 v122, v122, s55, v232
	v_med3_f32 v123, v123, s55, v232
	v_pk_add_f32 v[126:127], v[126:127], 1.0 op_sel_hi:[1,0]
	v_pk_add_f32 v[134:135], v[120:121], 1.0 op_sel_hi:[1,0]
	v_pk_add_f32 v[116:117], v[116:117], 1.0 op_sel_hi:[1,0]
	v_pk_add_f32 v[120:121], v[120:121], 1.0 op_sel_hi:[1,0] neg_lo:[1,0] neg_hi:[1,0]
	v_exp_f32_e32 v128, v128
	v_exp_f32_e32 v129, v129
	v_exp_f32_e32 v118, v118
	v_exp_f32_e32 v119, v119
	v_exp_f32_e32 v122, v122
	v_exp_f32_e32 v123, v123
	v_pk_mul_f32 v[126:127], v[126:127], v[134:135]
	v_exp_f32_e32 v130, v130
	v_exp_f32_e32 v131, v131
	v_pk_add_f32 v[128:129], v[128:129], 1.0 op_sel_hi:[1,0]
	v_pk_add_f32 v[136:137], v[122:123], 1.0 op_sel_hi:[1,0]
	v_pk_add_f32 v[118:119], v[118:119], 1.0 op_sel_hi:[1,0]
	v_pk_add_f32 v[122:123], v[122:123], 1.0 op_sel_hi:[1,0] neg_lo:[1,0] neg_hi:[1,0]
	v_rcp_f32_e32 v126, v126
	v_rcp_f32_e32 v127, v127
	v_rcp_f32_e32 v116, v116
	v_rcp_f32_e32 v117, v117
	v_pk_mul_f32 v[128:129], v[128:129], v[136:137]
	v_exp_f32_e32 v132, v132
	v_exp_f32_e32 v133, v133
	v_pk_mul_f32 v[120:121], v[120:121], v[126:127]
	v_pk_add_f32 v[130:131], v[130:131], 1.0 op_sel_hi:[1,0]
	v_rcp_f32_e32 v128, v128
	v_rcp_f32_e32 v129, v129
	v_rcp_f32_e32 v118, v118
	v_rcp_f32_e32 v119, v119
	v_pk_fma_f32 v[168:169], v[168:169], v[116:117], v[120:121]
	v_pk_mul_f32 v[122:123], v[122:123], v[128:129]
	v_pk_add_f32 v[132:133], v[132:133], 1.0 op_sel_hi:[1,0]
	v_pk_mul_f32 v[134:135], v[168:169], s[78:79]
	v_pk_fma_f32 v[170:171], v[170:171], v[118:119], v[122:123]
	v_med3_f32 v134, v134, s55, v232
	v_med3_f32 v135, v135, s55, v232
	v_pk_mul_f32 v[136:137], v[170:171], s[78:79]
	v_add_u32_e32 v122, 0x100, v166
	v_mov_b32_e32 v123, v114
	v_lshl_add_u64 v[122:123], v[122:123], 1, s[30:31]
	v_exp_f32_e32 v134, v134
	v_exp_f32_e32 v135, v135
	v_med3_f32 v136, v136, s55, v232
	v_med3_f32 v137, v137, s55, v232
	v_pk_add_f32 v[126:127], v[134:135], 1.0 op_sel_hi:[1,0]
	v_pk_add_f32 v[134:135], v[134:135], 1.0 op_sel_hi:[1,0] neg_lo:[1,0] neg_hi:[1,0]
	v_exp_f32_e32 v136, v136
	v_exp_f32_e32 v137, v137
	v_pk_mul_f32 v[130:131], v[130:131], v[126:127]
	v_pk_add_f32 v[128:129], v[136:137], 1.0 op_sel_hi:[1,0]
	v_pk_add_f32 v[136:137], v[136:137], 1.0 op_sel_hi:[1,0] neg_lo:[1,0] neg_hi:[1,0]
	v_rcp_f32_e32 v130, v130
	v_rcp_f32_e32 v131, v131
	v_pk_mul_f32 v[132:133], v[132:133], v[128:129]
	v_pk_mul_f32 v[134:135], v[134:135], v[130:131]
	v_rcp_f32_e32 v132, v132
	v_rcp_f32_e32 v133, v133
	v_cvt_pk_bf16_f32 v120, v134, v135
	v_pk_mul_f32 v[136:137], v[136:137], v[132:133]
	v_pk_mul_f32 v[134:135], v[162:163], v[134:135]
	v_cvt_pk_bf16_f32 v121, v136, v137
	v_cvt_pk_bf16_f32 v116, v134, v135
	v_pk_mul_f32 v[136:137], v[164:165], v[136:137]
	global_store_dwordx2 v[122:123], v[120:121], off
	v_cvt_pk_bf16_f32 v117, v136, v137
	ds_write_b64 v205, v[116:117] offset:4608
	s_and_b64 s[72:73], exec, s[6:7]
	s_cbranch_scc1 .Lpf_skip_3
	ds_read_b128 v[250:253], v199 offset:9216
	ds_read_b128 v[120:123], v198 offset:57600
	ds_read_b128 v[124:127], v199 offset:9344
	ds_read_b128 v[246:249], v199 offset:9280
	ds_read_b128 v[128:131], v199 offset:9408

.Lred_skip_3:
	s_nop 5
	v_exp_f32_e32 v142, v116
	v_med3_f32 v116, v124, s55, v232
	v_exp_f32_e32 v143, v116
	v_mfma_f32_16x16x32_bf16 v[128:131], v[102:105], v[134:137], v[130:133]
	v_exp_f32_e32 v124, v117
	v_exp_f32_e32 v115, v120
	v_exp_f32_e32 v117, v121
	v_med3_f32 v121, v125, s55, v232
	v_exp_f32_e32 v125, v121
	v_mfma_f32_16x16x32_bf16 v[128:131], v[106:109], v[138:141], v[128:131]
	v_add_f32_e32 v115, 1.0, v115
	v_pk_add_f32 v[132:133], v[142:143], 1.0 op_sel_hi:[1,0]
	v_rcp_f32_e32 v120, v115
	v_mul_f32_e32 v115, v132, v133
	v_pk_add_f32 v[134:135], v[124:125], 1.0 op_sel_hi:[1,0]
	s_nop 2
	v_exp_f32_e32 v116, v128
	v_rcp_f32_e32 v128, v115
	v_add_f32_e32 v115, 1.0, v117
	v_mul_f32_e32 v117, v134, v135
	v_exp_f32_e32 v132, v129
	v_rcp_f32_e32 v129, v117
	v_rcp_f32_e32 v121, v115
	v_mov_b32_e32 v124, v143
	v_pk_add_f32 v[124:125], v[124:125], 1.0 op_sel_hi:[1,0] neg_lo:[1,0] neg_hi:[1,0]
	s_nop 0
	v_pk_mul_f32 v[124:125], v[124:125], v[128:129]
	s_nop 0
	v_pk_fma_f32 v[168:169], v[168:169], v[120:121], v[124:125]
	s_nop 0
	v_mul_f32_e32 v115, 0xc038aa3b, v168
	v_med3_f32 v115, v115, s55, v232
	v_exp_f32_e32 v117, v115
	v_mul_f32_e32 v115, 0xc038aa3b, v169
	v_med3_f32 v115, v115, s55, v232
	v_exp_f32_e32 v133, v115
	v_pk_add_f32 v[120:121], v[116:117], 1.0 op_sel_hi:[1,0]
	v_pk_add_f32 v[124:125], v[132:133], 1.0 op_sel_hi:[1,0]
	v_mul_f32_e32 v115, v120, v121
	v_rcp_f32_e32 v120, v115
	v_mul_f32_e32 v115, v124, v125
	v_exp_f32_e32 v124, v118
	v_med3_f32 v118, v126, s55, v232
	v_rcp_f32_e32 v121, v115
	v_exp_f32_e32 v115, v122
	v_exp_f32_e32 v125, v118
	v_exp_f32_e32 v126, v119
	v_exp_f32_e32 v119, v123
	v_med3_f32 v123, v127, s55, v232
	v_exp_f32_e32 v127, v123
	v_add_f32_e32 v115, 1.0, v115
	v_pk_add_f32 v[128:129], v[124:125], 1.0 op_sel_hi:[1,0]
	v_exp_f32_e32 v118, v130
	v_rcp_f32_e32 v122, v115
	v_mul_f32_e32 v115, v128, v129
	v_exp_f32_e32 v124, v131
	v_pk_add_f32 v[130:131], v[126:127], 1.0 op_sel_hi:[1,0]
	v_rcp_f32_e32 v128, v115
	v_add_f32_e32 v115, 1.0, v119
	v_mul_f32_e32 v119, v130, v131
	v_rcp_f32_e32 v129, v119
	v_rcp_f32_e32 v123, v115
	v_mov_b32_e32 v126, v125
	v_pk_add_f32 v[126:127], v[126:127], 1.0 op_sel_hi:[1,0] neg_lo:[1,0] neg_hi:[1,0]
	v_mov_b32_e32 v132, v117
	v_pk_mul_f32 v[126:127], v[126:127], v[128:129]
	v_pk_add_f32 v[116:117], v[132:133], 1.0 op_sel_hi:[1,0] neg_lo:[1,0] neg_hi:[1,0]
	v_pk_fma_f32 v[170:171], v[170:171], v[122:123], v[126:127]
	v_pk_mul_f32 v[116:117], v[116:117], v[120:121]
	v_mul_f32_e32 v115, 0xc038aa3b, v170
	v_med3_f32 v115, v115, s55, v232
	v_exp_f32_e32 v119, v115
	v_mul_f32_e32 v115, 0xc038aa3b, v171
	v_med3_f32 v115, v115, s55, v232
	v_exp_f32_e32 v125, v115
	v_pk_add_f32 v[122:123], v[118:119], 1.0 op_sel_hi:[1,0]
	v_cvt_pk_bf16_f32 v120, v116, v117
	v_mul_f32_e32 v115, v122, v123
	v_pk_add_f32 v[126:127], v[124:125], 1.0 op_sel_hi:[1,0]
	v_rcp_f32_e32 v122, v115
	v_mul_f32_e32 v115, v126, v127
	v_rcp_f32_e32 v123, v115
	v_mov_b32_e32 v124, v119
	v_pk_add_f32 v[118:119], v[124:125], 1.0 op_sel_hi:[1,0] neg_lo:[1,0] neg_hi:[1,0]
	s_nop 0
	v_pk_mul_f32 v[118:119], v[118:119], v[122:123]
	v_add_u32_e32 v122, 0x180, v166
	v_mov_b32_e32 v123, v114
	v_cvt_pk_bf16_f32 v121, v118, v119
	v_lshl_add_u64 v[122:123], v[122:123], 1, s[30:31]
	global_store_dwordx2 v[122:123], v[120:121], off
	s_cbranch_vccnz .LBB1_42
	v_pk_mul_f32 v[116:117], v[162:163], v[116:117]
	v_pk_mul_f32 v[118:119], v[164:165], v[118:119]
	v_cvt_pk_bf16_f32 v116, v116, v117
	v_cvt_pk_bf16_f32 v117, v118, v119
	ds_write_b64 v205, v[116:117]
	s_branch .LBB1_42
